# v3 + s_setprio 2 around the MFMA parts of the scan output pass (both wave roles), 0 elsewhere
# baseline (speedup 1.0000x reference)
.LBB0_414:
	s_setprio 0
	s_waitcnt lgkmcnt(0)
	s_waitcnt lgkmcnt(0)
	s_barrier
	global_load_dwordx4 v[10:13], v[204:205], off
	global_load_dwordx4 v[16:19], v[204:205], off offset:16
	global_load_dwordx4 v[20:23], v[204:205], off offset:32
	global_load_dwordx4 v[24:27], v[204:205], off offset:48
	v_lshl_add_u32 v0, v212, 2, 0
	v_mad_u64_u32 v[28:29], s[0:1], v212, s64, v[14:15]
	s_waitcnt vmcnt(5)
	v_lshlrev_b32_e32 v30, 16, v6
	v_and_b32_e32 v31, 0xffff0000, v6
	v_lshlrev_b32_e32 v32, 16, v7
	v_and_b32_e32 v33, 0xffff0000, v7
	v_lshlrev_b32_e32 v34, 16, v8
	v_and_b32_e32 v35, 0xffff0000, v8
	v_lshlrev_b32_e32 v36, 16, v9
	v_and_b32_e32 v37, 0xffff0000, v9
	s_waitcnt vmcnt(4)
	v_lshlrev_b32_e32 v38, 16, v2
	v_and_b32_e32 v39, 0xffff0000, v2
	v_lshlrev_b32_e32 v40, 16, v3
	v_and_b32_e32 v41, 0xffff0000, v3
	v_lshlrev_b32_e32 v42, 16, v4
	v_and_b32_e32 v43, 0xffff0000, v4
	v_lshlrev_b32_e32 v44, 16, v5
	v_and_b32_e32 v45, 0xffff0000, v5
	ds_read_b128 v[2:5], v28
	v_add_u32_e32 v0, 0x27800, v0
	ds_read_b128 v[6:9], v28 offset:16
	ds_read2st64_b32 v[28:29], v0 offset1:1
	ds_read2st64_b32 v[46:47], v0 offset0:2 offset1:3
	s_add_i32 s74, s74, 1
	s_add_u32 s22, s22, 0x20000
	s_waitcnt lgkmcnt(3)
	v_lshlrev_b32_e32 v48, 16, v2
	s_waitcnt lgkmcnt(1)
	v_mov_b32_e32 v56, v28
	s_waitcnt lgkmcnt(0)
	v_mov_b32_e32 v57, v46
	v_mov_b32_e32 v46, v29
	v_pk_add_f32 v[28:29], v[56:57], v[46:47]
	v_and_b32_e32 v49, 0xffff0000, v2
	v_add_f32_e32 v0, v28, v29
	v_fmamk_f32 v0, v0, 0x3c000000, v219
	v_rsq_f32_e32 v0, v0
	v_lshlrev_b32_e32 v2, 16, v3
	v_and_b32_e32 v3, 0xffff0000, v3
	v_lshlrev_b32_e32 v50, 16, v4
	v_and_b32_e32 v51, 0xffff0000, v4
	v_lshlrev_b32_e32 v4, 16, v5
	v_and_b32_e32 v5, 0xffff0000, v5
	v_lshlrev_b32_e32 v52, 16, v6
	v_and_b32_e32 v53, 0xffff0000, v6
	v_lshlrev_b32_e32 v6, 16, v7
	v_and_b32_e32 v7, 0xffff0000, v7
	v_pk_mul_f32 v[2:3], v[0:1], v[2:3] op_sel_hi:[0,1]
	v_pk_mul_f32 v[28:29], v[0:1], v[48:49] op_sel_hi:[0,1]
	v_pk_mul_f32 v[4:5], v[0:1], v[4:5] op_sel_hi:[0,1]
	v_pk_mul_f32 v[46:47], v[0:1], v[50:51] op_sel_hi:[0,1]
	v_pk_mul_f32 v[6:7], v[0:1], v[6:7] op_sel_hi:[0,1]
	v_pk_mul_f32 v[48:49], v[0:1], v[52:53] op_sel_hi:[0,1]
	v_lshlrev_b32_e32 v54, 16, v8
	v_and_b32_e32 v55, 0xffff0000, v8
	v_lshlrev_b32_e32 v8, 16, v9
	v_and_b32_e32 v9, 0xffff0000, v9
	v_pk_mul_f32 v[8:9], v[0:1], v[8:9] op_sel_hi:[0,1]
	v_pk_mul_f32 v[50:51], v[0:1], v[54:55] op_sel_hi:[0,1]
	s_addc_u32 s23, s23, 0
	v_mov_b64_e32 v[64:65], v[80:81]
	v_mov_b64_e32 v[160:161], v[180:181]
	v_mov_b64_e32 v[176:177], v[196:197]
	v_mov_b64_e32 v[172:173], v[200:201]
	v_mov_b64_e32 v[168:169], v[184:185]
	v_mov_b64_e32 v[164:165], v[192:193]
	s_cmp_eq_u32 s22, 0x100000
	v_mov_b64_e32 v[66:67], v[82:83]
	v_mov_b64_e32 v[68:69], v[84:85]
	v_mov_b64_e32 v[70:71], v[86:87]
	v_mov_b64_e32 v[72:73], v[88:89]
	v_mov_b64_e32 v[74:75], v[90:91]
	v_mov_b64_e32 v[76:77], v[92:93]
	v_mov_b64_e32 v[78:79], v[94:95]
	v_mov_b64_e32 v[162:163], v[182:183]
	v_mov_b64_e32 v[178:179], v[198:199]
	v_mov_b64_e32 v[174:175], v[202:203]
	v_mov_b64_e32 v[170:171], v[186:187]
	v_mov_b64_e32 v[166:167], v[194:195]
	s_waitcnt vmcnt(3)
	v_pk_mul_f32 v[10:11], v[10:11], v[28:29]
	v_pk_mul_f32 v[2:3], v[12:13], v[2:3]
	s_waitcnt vmcnt(2)
	v_pk_mul_f32 v[12:13], v[16:17], v[46:47]
	v_pk_mul_f32 v[4:5], v[18:19], v[4:5]
	s_waitcnt vmcnt(1)
	v_pk_mul_f32 v[16:17], v[20:21], v[48:49]
	v_pk_mul_f32 v[6:7], v[22:23], v[6:7]
	v_pk_mul_f32 v[20:21], v[2:3], v[32:33]
	v_pk_mul_f32 v[2:3], v[10:11], v[30:31]
	v_pk_mul_f32 v[10:11], v[4:5], v[36:37]
	v_pk_mul_f32 v[4:5], v[12:13], v[34:35]
	v_pk_mul_f32 v[6:7], v[6:7], v[40:41]
	v_cvt_pk_bf16_f32 v2, v2, v3
	v_cvt_pk_bf16_f32 v3, v20, v21
	v_pk_mul_f32 v[12:13], v[16:17], v[38:39]
	v_cvt_pk_bf16_f32 v4, v4, v5
	v_cvt_pk_bf16_f32 v5, v10, v11
	global_store_dwordx4 v[210:211], v[2:5], off
	s_waitcnt vmcnt(1)
	v_pk_mul_f32 v[18:19], v[24:25], v[50:51]
	v_pk_mul_f32 v[8:9], v[26:27], v[8:9]
	v_cvt_pk_bf16_f32 v2, v12, v13
	v_cvt_pk_bf16_f32 v3, v6, v7
	v_add_co_u32_e32 v6, vcc, s61, v208
	v_pk_mul_f32 v[8:9], v[8:9], v[44:45]
	s_nop 0
	v_addc_co_u32_e32 v7, vcc, 0, v209, vcc
	v_pk_mul_f32 v[16:17], v[18:19], v[42:43]
	v_mov_b64_e32 v[48:49], v[128:129]
	v_cvt_pk_bf16_f32 v4, v16, v17
	v_cvt_pk_bf16_f32 v5, v8, v9
	global_store_dwordx4 v[6:7], v[2:5], off offset:16
	s_waitcnt lgkmcnt(0)
	v_mov_b64_e32 v[32:33], v[112:113]
	v_mov_b64_e32 v[16:17], v[96:97]
	v_mov_b64_e32 v[10:11], v[188:189]
	v_mov_b64_e32 v[50:51], v[130:131]
	v_mov_b64_e32 v[52:53], v[132:133]
	v_mov_b64_e32 v[54:55], v[134:135]
	v_mov_b64_e32 v[56:57], v[136:137]
	v_mov_b64_e32 v[58:59], v[138:139]
	v_mov_b64_e32 v[60:61], v[140:141]
	v_mov_b64_e32 v[62:63], v[142:143]
	v_mov_b64_e32 v[34:35], v[114:115]
	v_mov_b64_e32 v[36:37], v[116:117]
	v_mov_b64_e32 v[38:39], v[118:119]
	v_mov_b64_e32 v[40:41], v[120:121]
	v_mov_b64_e32 v[42:43], v[122:123]
	v_mov_b64_e32 v[44:45], v[124:125]
	v_mov_b64_e32 v[46:47], v[126:127]
	v_mov_b64_e32 v[18:19], v[98:99]
	v_mov_b64_e32 v[20:21], v[100:101]
	v_mov_b64_e32 v[22:23], v[102:103]
	v_mov_b64_e32 v[24:25], v[104:105]
	v_mov_b64_e32 v[26:27], v[106:107]
	v_mov_b64_e32 v[28:29], v[108:109]
	v_mov_b64_e32 v[30:31], v[110:111]
	v_mov_b64_e32 v[12:13], v[190:191]
	s_barrier
	s_cbranch_scc1 .LBB0_406
.LBB0_415:
	v_mov_b32_e32 v212, v15
	s_and_b32 s0, s74, 1
	v_ashrrev_i32_e32 v213, 31, v212
	v_lshlrev_b64 v[2:3], 11, v[212:213]
	v_lshl_add_u64 v[2:3], s[22:23], 0, v[2:3]
	v_lshl_add_u64 v[208:209], v[206:207], 0, v[2:3]
	v_add_co_u32_e32 v2, vcc, 0x2e200000, v208
	v_lshl_add_u64 v[210:211], v[208:209], 0, s[12:13]
	s_nop 0
	v_addc_co_u32_e32 v3, vcc, 0, v209, vcc
	global_load_dwordx4 v[6:9], v[2:3], off
	s_nop 0
	global_load_dwordx4 v[2:5], v[210:211], off offset:16
	s_mul_i32 s1, s0, 0x11a00
	s_xor_b32 s0, s0, 1
	s_mul_i32 s0, s0, 0x11a00
	s_add_i32 s76, s1, 0
	s_add_i32 s78, s0, 0
	s_mov_b64 s[0:1], -1
	s_and_b64 vcc, exec, s[6:7]
	s_cbranch_vccz .LBB0_429
	s_setprio 2
	v_mov_b32_e32 v0, v214
	v_mov_b32_e32 v80, s76
	v_and_b32_e32 v188, 31, v0
	v_bfe_u32 v189, v0, 5, 1
	v_or_b32_e32 v0, s37, v188
	v_mad_u32_u24 v139, v0, s64, v80
	v_lshlrev_b32_e32 v137, 4, v189
	v_add_u32_e32 v80, v139, v137
	ds_read_b128 v[124:127], v80
	ds_read_b128 v[120:123], v80 offset:32
	ds_read_b128 v[116:119], v80 offset:64
	ds_read_b128 v[112:115], v80 offset:96
	ds_read_b128 v[108:111], v80 offset:128
	ds_read_b128 v[104:107], v80 offset:160
	ds_read_b128 v[100:103], v80 offset:192
	ds_read_b128 v[96:99], v80 offset:224
	v_or_b32_e32 v80, s8, v188
	v_mul_lo_u32 v80, v80, s60
	v_add_u32_e32 v138, s76, v80
	v_lshlrev_b32_e32 v190, 3, v189
	v_add_u32_e32 v136, s76, v137
	v_add_u32_e32 v128, v138, v190
	s_and_b64 vcc, exec, s[10:11]
	s_cbranch_vccz .LBB0_442
	v_mad_u32_u24 v84, v188, s64, v136
	ds_read_b128 v[80:83], v84 offset:17408
	ds_read_b128 v[130:133], v84 offset:17440
	ds_read_b128 v[140:143], v84 offset:17472
	ds_read_b128 v[144:147], v84 offset:17504
	ds_read_b128 v[148:151], v84 offset:17536
	ds_read_b128 v[152:155], v84 offset:17568
	ds_read_b128 v[156:159], v84 offset:17600
	ds_read_b128 v[180:183], v84 offset:17632
	v_add_u32_e32 v84, 0xd000, v128
	ds_read2_b64 v[184:187], v84 offset1:2
	ds_read2_b64 v[192:195], v84 offset0:4 offset1:6
	s_waitcnt lgkmcnt(0)
	s_waitcnt lgkmcnt(9)
	v_mfma_f32_32x32x16_bf16 v[80:95], v[80:83], v[124:127], 0
	s_waitcnt lgkmcnt(8)
	v_mfma_f32_32x32x16_bf16 v[80:95], v[130:133], v[120:123], v[80:95]
	s_waitcnt lgkmcnt(7)
	v_mfma_f32_32x32x16_bf16 v[80:95], v[140:143], v[116:119], v[80:95]
	s_waitcnt lgkmcnt(6)
	v_mfma_f32_32x32x16_bf16 v[80:95], v[144:147], v[112:115], v[80:95]
	s_waitcnt lgkmcnt(5)
	v_mfma_f32_32x32x16_bf16 v[80:95], v[148:151], v[108:111], v[80:95]
	s_waitcnt lgkmcnt(4)
	v_mfma_f32_32x32x16_bf16 v[80:95], v[152:155], v[104:107], v[80:95]
	s_waitcnt lgkmcnt(3)
	v_mfma_f32_32x32x16_bf16 v[80:95], v[156:159], v[100:103], v[80:95]
	s_waitcnt lgkmcnt(2)
	v_mfma_f32_32x32x16_bf16 v[80:95], v[180:183], v[96:99], v[80:95]
	s_nop 11
	v_cvt_pk_bf16_f32 v80, v80, v81
	v_cvt_pk_bf16_f32 v81, v82, v83
	v_cvt_pk_bf16_f32 v82, v84, v85
	v_cvt_pk_bf16_f32 v83, v86, v87
	s_waitcnt lgkmcnt(1)
	s_nop 0
	v_mfma_f32_32x32x16_bf16 v[144:159], v[184:187], v[80:83], 0
	v_cvt_pk_bf16_f32 v80, v88, v89
	v_cvt_pk_bf16_f32 v81, v90, v91
	v_cvt_pk_bf16_f32 v82, v92, v93
	v_cvt_pk_bf16_f32 v83, v94, v95
	s_waitcnt lgkmcnt(0)
	s_nop 0
	v_mfma_f32_32x32x16_bf16 v[144:159], v[192:195], v[80:83], v[144:159]
	s_mov_b32 s0, 1
	s_cbranch_execnz .LBB0_419

.LBB0_423:
	s_or_b64 exec, exec, s[0:1]
	v_mul_u32_u24_e32 v0, 0x110, v0
	v_add3_u32 v0, s39, v0, v190
	v_cvt_pk_bf16_f32 v144, v144, v145
	v_cvt_pk_bf16_f32 v145, v146, v147
	v_cvt_pk_bf16_f32 v146, v148, v149
	v_cvt_pk_bf16_f32 v147, v150, v151
	s_setprio 0
	s_waitcnt vmcnt(2)
	v_mov_b64_e32 v[198:199], v[178:179]
	v_mov_b64_e32 v[202:203], v[174:175]
	v_mov_b64_e32 v[186:187], v[170:171]
	v_mov_b64_e32 v[194:195], v[166:167]
	s_waitcnt lgkmcnt(0)
	v_mov_b64_e32 v[182:183], v[162:163]
	v_mov_b64_e32 v[190:191], v[12:13]
	ds_write2_b64 v0, v[144:145], v[146:147] offset1:2
	v_cvt_pk_bf16_f32 v144, v152, v153
	v_cvt_pk_bf16_f32 v145, v154, v155
	v_cvt_pk_bf16_f32 v146, v156, v157
	v_cvt_pk_bf16_f32 v147, v158, v159
	s_cmp_eq_u32 s22, 0xe0000
	v_mov_b64_e32 v[196:197], v[176:177]
	v_mov_b64_e32 v[200:201], v[172:173]
	v_mov_b64_e32 v[184:185], v[168:169]
	v_mov_b64_e32 v[192:193], v[164:165]
	v_mov_b64_e32 v[180:181], v[160:161]
	v_mov_b64_e32 v[188:189], v[10:11]
	ds_write2_b64 v0, v[144:145], v[146:147] offset0:4 offset1:6
	s_cbranch_scc1 .LBB0_428
	v_cvt_f32_f16_e32 v144, v160
	v_cvt_f32_f16_sdwa v145, v160 dst_sel:DWORD dst_unused:UNUSED_PAD src0_sel:WORD_1
	v_cvt_f32_f16_e32 v150, v161
	v_cvt_f32_f16_sdwa v151, v161 dst_sel:DWORD dst_unused:UNUSED_PAD src0_sel:WORD_1
	v_cvt_f32_f16_e32 v155, v162
	v_add_f32_e32 v192, 0, v144
	v_cvt_f32_f16_sdwa v156, v162 dst_sel:DWORD dst_unused:UNUSED_PAD src0_sel:WORD_1
	v_add_f32_e32 v193, v192, v145
	v_cvt_f32_f16_e32 v159, v163
	v_add_f32_e32 v194, v193, v150
	v_cvt_f32_f16_sdwa v180, v163 dst_sel:DWORD dst_unused:UNUSED_PAD src0_sel:WORD_1
	v_add_f32_e32 v195, v194, v151
	v_cvt_f32_f16_e32 v183, v10
	v_add_f32_e32 v196, v195, v155
	v_cvt_f32_f16_sdwa v184, v10 dst_sel:DWORD dst_unused:UNUSED_PAD src0_sel:WORD_1
	v_add_f32_e32 v197, v196, v156
	v_cvt_f32_f16_e32 v186, v11
	v_add_f32_e32 v198, v197, v159
	v_cvt_f32_f16_sdwa v187, v11 dst_sel:DWORD dst_unused:UNUSED_PAD src0_sel:WORD_1
	v_add_f32_e32 v199, v198, v180
	v_cvt_f32_f16_e32 v188, v12
	v_add_f32_e32 v200, v199, v183
	v_cvt_f32_f16_sdwa v189, v12 dst_sel:DWORD dst_unused:UNUSED_PAD src0_sel:WORD_1
	v_add_f32_e32 v201, v200, v184
	v_cvt_f32_f16_e32 v190, v13
	v_add_f32_e32 v202, v201, v186
	v_cvt_f32_f16_sdwa v191, v13 dst_sel:DWORD dst_unused:UNUSED_PAD src0_sel:WORD_1
	v_add_f32_e32 v203, v202, v187
	v_add_f32_e32 v213, v203, v188
	v_add_f32_e32 v220, v213, v189
	v_add_f32_e32 v221, v220, v190
	v_add_f32_e32 v222, v221, v191
	ds_bpermute_b32 v149, v215, v222
	v_mov_b32_e32 v148, v214
	v_mul_f32_e32 v144, 0x3fb8aa3b, v144
	v_and_b32_e32 v0, 3, v148
	s_waitcnt lgkmcnt(0)
	v_add_f32_e32 v149, v222, v149
	v_cmp_eq_u32_e32 vcc, 0, v0
	v_cmp_lt_u32_e64 s[2:3], 1, v0
	v_exp_f32_e32 v144, v144
	v_cndmask_b32_e32 v149, v149, v222, vcc
	ds_bpermute_b32 v226, v216, v149
	v_lshlrev_b32_e32 v146, 16, v164
	v_sub_f32_e32 v144, 1.0, v144
	v_mul_f32_e32 v145, 0x3fb8aa3b, v145
	v_exp_f32_e32 v145, v145
	s_waitcnt lgkmcnt(0)
	v_add_f32_e32 v226, v149, v226
	v_cndmask_b32_e64 v226, v149, v226, s[2:3]
	ds_bpermute_b32 v149, v217, v226
	v_sub_f32_e32 v226, v226, v222
	v_add_f32_e32 v192, v192, v226
	v_mul_f32_e32 v232, 0x3fb8aa3b, v192
	v_max_f32_e32 v233, 0xc2a00000, v192
	s_waitcnt lgkmcnt(0)
	v_sub_f32_e32 v192, v149, v192
	v_mul_f32_e32 v233, 0xbfb8aa3b, v233
	v_mul_f32_e32 v192, 0x3fb8aa3b, v192
	v_exp_f32_e32 v232, v232
	v_exp_f32_e32 v233, v233
	v_exp_f32_e32 v192, v192
	v_ashrrev_i32_e32 v154, 2, v148
	v_mul_f32_e32 v146, v232, v146
	v_mul_f32_e32 v232, v144, v233
	v_mul_f32_e32 v144, v144, v192
	v_add_f32_e32 v192, v193, v226
	v_mul_f32_e32 v193, 0x3fb8aa3b, v192
	v_max_f32_e32 v233, 0xc2a00000, v192
	v_sub_f32_e32 v192, v149, v192
	v_mul_f32_e32 v233, 0xbfb8aa3b, v233
	v_mul_f32_e32 v192, 0x3fb8aa3b, v192
	v_exp_f32_e32 v193, v193
	v_exp_f32_e32 v233, v233
	v_exp_f32_e32 v192, v192
	v_and_b32_e32 v147, 0xffff0000, v164
	v_sub_f32_e32 v145, 1.0, v145
	v_lshlrev_b32_e32 v231, 1, v154
	v_mul_f32_e32 v147, v193, v147
	v_mul_f32_e32 v193, v145, v233
	v_mul_f32_e32 v145, v145, v192
	v_mul_u32_u24_e32 v192, 0x1100, v0
	v_cvt_pk_bf16_f32 v146, v146, v147
	v_add3_u32 v192, s78, v231, v192
	v_cvt_pk_bf16_f32 v147, v232, v193
	ds_write_b16 v192, v146
	ds_write_b16_d16_hi v192, v146 offset:272
	ds_write_b16 v192, v147 offset:17408
	ds_write_b16_d16_hi v192, v147 offset:17680
	v_cvt_pk_bf16_f32 v144, v144, v145
	v_add_f32_e32 v145, v194, v226
	v_mul_f32_e32 v146, 0x3fb8aa3b, v150
	v_mul_f32_e32 v147, 0x3fb8aa3b, v145
	v_max_f32_e32 v150, 0xc2a00000, v145
	v_sub_f32_e32 v145, v149, v145
	v_exp_f32_e32 v146, v146
	v_mul_f32_e32 v150, 0xbfb8aa3b, v150
	v_mul_f32_e32 v145, 0x3fb8aa3b, v145
	v_exp_f32_e32 v150, v150
	v_exp_f32_e32 v145, v145
	v_exp_f32_e32 v147, v147
	v_sub_f32_e32 v146, 1.0, v146
	v_lshlrev_b32_e32 v152, 16, v165
	v_mul_f32_e32 v150, v146, v150
	v_mul_f32_e32 v145, v146, v145
	v_add_f32_e32 v146, v195, v226
	v_mul_f32_e32 v147, v147, v152
	v_mul_f32_e32 v151, 0x3fb8aa3b, v151
	v_mul_f32_e32 v152, 0x3fb8aa3b, v146
	v_max_f32_e32 v193, 0xc2a00000, v146
	v_sub_f32_e32 v146, v149, v146
	v_exp_f32_e32 v151, v151
	v_mul_f32_e32 v146, 0x3fb8aa3b, v146
	v_exp_f32_e32 v152, v152
	v_mul_f32_e32 v193, 0xbfb8aa3b, v193
	v_exp_f32_e32 v146, v146
	v_exp_f32_e32 v193, v193
	v_and_b32_e32 v153, 0xffff0000, v165
	v_sub_f32_e32 v151, 1.0, v151
	v_mul_f32_e32 v152, v152, v153
	v_mul_f32_e32 v146, v151, v146
	v_cvt_pk_bf16_f32 v147, v147, v152
	v_mul_f32_e32 v153, v151, v193
	v_cvt_pk_bf16_f32 v150, v150, v153
	ds_write_b16 v192, v147 offset:544
	ds_write_b16_d16_hi v192, v147 offset:816
	ds_write_b16 v192, v150 offset:17952
	ds_write_b16_d16_hi v192, v150 offset:18224
	v_cvt_pk_bf16_f32 v145, v145, v146
	v_add_f32_e32 v146, v196, v226
	v_mul_f32_e32 v147, 0x3fb8aa3b, v155
	v_mul_f32_e32 v150, 0x3fb8aa3b, v146
	v_max_f32_e32 v151, 0xc2a00000, v146
	v_sub_f32_e32 v146, v149, v146
	v_exp_f32_e32 v147, v147
	v_mul_f32_e32 v151, 0xbfb8aa3b, v151
	v_mul_f32_e32 v146, 0x3fb8aa3b, v146
	v_exp_f32_e32 v151, v151
	v_exp_f32_e32 v146, v146
	v_sub_f32_e32 v147, 1.0, v147
	v_mul_f32_e32 v152, 0x3fb8aa3b, v156
	v_mul_f32_e32 v151, v147, v151
	v_mul_f32_e32 v146, v147, v146
	v_add_f32_e32 v147, v197, v226
	v_mul_f32_e32 v153, 0x3fb8aa3b, v147
	v_max_f32_e32 v155, 0xc2a00000, v147
	v_sub_f32_e32 v147, v149, v147
	v_exp_f32_e32 v150, v150
	v_exp_f32_e32 v152, v152
	v_mul_f32_e32 v147, 0x3fb8aa3b, v147
	v_exp_f32_e32 v153, v153
	v_mul_f32_e32 v155, 0xbfb8aa3b, v155
	v_exp_f32_e32 v147, v147
	v_exp_f32_e32 v155, v155
	v_lshlrev_b32_e32 v157, 16, v166
	v_and_b32_e32 v158, 0xffff0000, v166
	v_mul_f32_e32 v150, v150, v157
	v_sub_f32_e32 v152, 1.0, v152
	v_mul_f32_e32 v153, v153, v158
	v_mul_f32_e32 v147, v152, v147
	v_cvt_pk_bf16_f32 v150, v150, v153
	v_mul_f32_e32 v155, v152, v155
	v_cvt_pk_bf16_f32 v151, v151, v155
	ds_write_b16 v192, v150 offset:1088
	ds_write_b16_d16_hi v192, v150 offset:1360
	ds_write_b16 v192, v151 offset:18496
	ds_write_b16_d16_hi v192, v151 offset:18768
	v_cvt_pk_bf16_f32 v146, v146, v147
	v_add_f32_e32 v147, v198, v226
	v_mul_f32_e32 v150, 0x3fb8aa3b, v159
	v_mul_f32_e32 v151, 0x3fb8aa3b, v147
	v_max_f32_e32 v152, 0xc2a00000, v147
	v_sub_f32_e32 v147, v149, v147
	v_exp_f32_e32 v150, v150
	v_mul_f32_e32 v152, 0xbfb8aa3b, v152
	v_mul_f32_e32 v147, 0x3fb8aa3b, v147
	v_exp_f32_e32 v152, v152
	v_exp_f32_e32 v147, v147
	v_sub_f32_e32 v150, 1.0, v150
	v_mul_f32_e32 v153, 0x3fb8aa3b, v180
	v_mul_f32_e32 v152, v150, v152
	v_mul_f32_e32 v147, v150, v147
	v_add_f32_e32 v150, v199, v226
	v_mul_f32_e32 v155, 0x3fb8aa3b, v150
	v_max_f32_e32 v156, 0xc2a00000, v150
	v_sub_f32_e32 v150, v149, v150
	v_exp_f32_e32 v151, v151
	v_exp_f32_e32 v153, v153
	v_mul_f32_e32 v150, 0x3fb8aa3b, v150
	v_exp_f32_e32 v155, v155
	v_mul_f32_e32 v156, 0xbfb8aa3b, v156
	v_exp_f32_e32 v150, v150
	v_exp_f32_e32 v156, v156
	v_lshlrev_b32_e32 v181, 16, v167
	v_and_b32_e32 v182, 0xffff0000, v167
	v_mul_f32_e32 v151, v151, v181
	v_sub_f32_e32 v153, 1.0, v153
	v_mul_f32_e32 v155, v155, v182
	v_mul_f32_e32 v150, v153, v150
	v_cvt_pk_bf16_f32 v151, v151, v155
	v_mul_f32_e32 v156, v153, v156
	v_cvt_pk_bf16_f32 v152, v152, v156
	ds_write_b16 v192, v151 offset:1632
	ds_write_b16_d16_hi v192, v151 offset:1904
	ds_write_b16 v192, v152 offset:19040
	ds_write_b16_d16_hi v192, v152 offset:19312
	v_cvt_pk_bf16_f32 v147, v147, v150
	v_add_f32_e32 v150, v200, v226
	v_mul_f32_e32 v151, 0x3fb8aa3b, v183
	v_mul_f32_e32 v152, 0x3fb8aa3b, v150
	v_max_f32_e32 v153, 0xc2a00000, v150
	v_sub_f32_e32 v150, v149, v150
	v_exp_f32_e32 v151, v151
	v_mul_f32_e32 v153, 0xbfb8aa3b, v153
	v_mul_f32_e32 v150, 0x3fb8aa3b, v150
	v_exp_f32_e32 v153, v153
	v_exp_f32_e32 v150, v150
	v_sub_f32_e32 v151, 1.0, v151
	v_mul_f32_e32 v155, 0x3fb8aa3b, v184
	v_mul_f32_e32 v153, v151, v153
	v_mul_f32_e32 v150, v151, v150
	v_add_f32_e32 v151, v201, v226
	v_mul_f32_e32 v156, 0x3fb8aa3b, v151
	v_max_f32_e32 v157, 0xc2a00000, v151
	v_sub_f32_e32 v151, v149, v151
	v_exp_f32_e32 v152, v152
	v_exp_f32_e32 v155, v155
	v_mul_f32_e32 v151, 0x3fb8aa3b, v151
	v_exp_f32_e32 v156, v156
	v_mul_f32_e32 v157, 0xbfb8aa3b, v157
	v_exp_f32_e32 v151, v151
	v_exp_f32_e32 v157, v157
	v_lshlrev_b32_e32 v185, 16, v168
	v_and_b32_e32 v223, 0xffff0000, v168
	v_mul_f32_e32 v152, v152, v185
	v_sub_f32_e32 v155, 1.0, v155
	v_mul_f32_e32 v156, v156, v223
	v_mul_f32_e32 v151, v155, v151
	v_cvt_pk_bf16_f32 v152, v152, v156
	v_mul_f32_e32 v157, v155, v157
	v_cvt_pk_bf16_f32 v153, v153, v157
	ds_write_b16 v192, v152 offset:2176
	ds_write_b16_d16_hi v192, v152 offset:2448
	ds_write_b16 v192, v153 offset:19584
	ds_write_b16_d16_hi v192, v153 offset:19856
	v_cvt_pk_bf16_f32 v150, v150, v151
	v_add_f32_e32 v151, v202, v226
	v_mul_f32_e32 v152, 0x3fb8aa3b, v186
	v_mul_f32_e32 v153, 0x3fb8aa3b, v151
	v_max_f32_e32 v155, 0xc2a00000, v151
	v_sub_f32_e32 v151, v149, v151
	v_exp_f32_e32 v152, v152
	v_mul_f32_e32 v155, 0xbfb8aa3b, v155
	v_mul_f32_e32 v151, 0x3fb8aa3b, v151
	v_exp_f32_e32 v155, v155
	v_exp_f32_e32 v151, v151
	v_sub_f32_e32 v152, 1.0, v152
	v_mul_f32_e32 v156, 0x3fb8aa3b, v187
	v_mul_f32_e32 v155, v152, v155
	v_mul_f32_e32 v151, v152, v151
	v_add_f32_e32 v152, v203, v226
	v_mul_f32_e32 v157, 0x3fb8aa3b, v152
	v_max_f32_e32 v158, 0xc2a00000, v152
	v_sub_f32_e32 v152, v149, v152
	v_exp_f32_e32 v153, v153
	v_exp_f32_e32 v156, v156
	v_mul_f32_e32 v152, 0x3fb8aa3b, v152
	v_exp_f32_e32 v157, v157
	v_mul_f32_e32 v158, 0xbfb8aa3b, v158
	v_exp_f32_e32 v152, v152
	v_exp_f32_e32 v158, v158
	v_lshlrev_b32_e32 v224, 16, v169
	v_and_b32_e32 v225, 0xffff0000, v169
	v_mul_f32_e32 v153, v153, v224
	v_sub_f32_e32 v156, 1.0, v156
	v_mul_f32_e32 v157, v157, v225
	v_mul_f32_e32 v152, v156, v152
	v_cvt_pk_bf16_f32 v153, v153, v157
	v_mul_f32_e32 v158, v156, v158
	v_cvt_pk_bf16_f32 v155, v155, v158
	ds_write_b16 v192, v153 offset:2720
	ds_write_b16_d16_hi v192, v153 offset:2992
	ds_write_b16 v192, v155 offset:20128
	ds_write_b16_d16_hi v192, v155 offset:20400
	v_cvt_pk_bf16_f32 v151, v151, v152
	v_add_f32_e32 v152, v213, v226
	v_mul_f32_e32 v153, 0x3fb8aa3b, v188
	v_mul_f32_e32 v155, 0x3fb8aa3b, v152
	v_max_f32_e32 v156, 0xc2a00000, v152
	v_sub_f32_e32 v152, v149, v152
	v_exp_f32_e32 v153, v153
	v_mul_f32_e32 v156, 0xbfb8aa3b, v156
	v_mul_f32_e32 v152, 0x3fb8aa3b, v152
	v_exp_f32_e32 v156, v156
	v_exp_f32_e32 v152, v152
	v_sub_f32_e32 v153, 1.0, v153
	v_mul_f32_e32 v157, 0x3fb8aa3b, v189
	v_mul_f32_e32 v156, v153, v156
	v_mul_f32_e32 v152, v153, v152
	v_add_f32_e32 v153, v220, v226
	v_mul_f32_e32 v158, 0x3fb8aa3b, v153
	v_max_f32_e32 v159, 0xc2a00000, v153
	v_sub_f32_e32 v153, v149, v153
	v_exp_f32_e32 v155, v155
	v_exp_f32_e32 v157, v157
	v_mul_f32_e32 v153, 0x3fb8aa3b, v153
	v_exp_f32_e32 v158, v158
	v_mul_f32_e32 v159, 0xbfb8aa3b, v159
	v_exp_f32_e32 v153, v153
	v_exp_f32_e32 v159, v159
	v_lshlrev_b32_e32 v227, 16, v170
	v_and_b32_e32 v228, 0xffff0000, v170
	v_mul_f32_e32 v155, v155, v227
	v_sub_f32_e32 v157, 1.0, v157
	v_mul_f32_e32 v158, v158, v228
	v_mul_f32_e32 v153, v157, v153
	v_cvt_pk_bf16_f32 v155, v155, v158
	v_mul_f32_e32 v159, v157, v159
	v_cvt_pk_bf16_f32 v156, v156, v159
	ds_write_b16 v192, v155 offset:3264
	ds_write_b16_d16_hi v192, v155 offset:3536
	ds_write_b16 v192, v156 offset:20672
	ds_write_b16_d16_hi v192, v156 offset:20944
	v_cvt_pk_bf16_f32 v152, v152, v153
	v_add_f32_e32 v153, v221, v226
	v_mul_f32_e32 v155, 0x3fb8aa3b, v190
	v_mul_f32_e32 v156, 0x3fb8aa3b, v153
	v_max_f32_e32 v157, 0xc2a00000, v153
	v_sub_f32_e32 v153, v149, v153
	v_exp_f32_e32 v155, v155
	v_mul_f32_e32 v157, 0xbfb8aa3b, v157
	v_mul_f32_e32 v153, 0x3fb8aa3b, v153
	v_exp_f32_e32 v157, v157
	v_exp_f32_e32 v153, v153
	v_sub_f32_e32 v155, 1.0, v155
	v_mul_f32_e32 v158, 0x3fb8aa3b, v191
	v_mul_f32_e32 v157, v155, v157
	v_mul_f32_e32 v153, v155, v153
	v_add_f32_e32 v155, v222, v226
	v_mul_f32_e32 v159, 0x3fb8aa3b, v155
	v_max_f32_e32 v180, 0xc2a00000, v155
	v_sub_f32_e32 v155, v149, v155
	v_exp_f32_e32 v156, v156
	v_exp_f32_e32 v158, v158
	v_mul_f32_e32 v155, 0x3fb8aa3b, v155
	v_exp_f32_e32 v159, v159
	v_mul_f32_e32 v180, 0xbfb8aa3b, v180
	v_exp_f32_e32 v155, v155
	v_exp_f32_e32 v180, v180
	v_lshlrev_b32_e32 v229, 16, v171
	v_and_b32_e32 v230, 0xffff0000, v171
	v_mul_f32_e32 v156, v156, v229
	v_sub_f32_e32 v158, 1.0, v158
	v_mul_f32_e32 v159, v159, v230
	v_mul_f32_e32 v155, v158, v155
	v_cvt_pk_bf16_f32 v156, v156, v159
	v_mul_f32_e32 v180, v158, v180
	v_cvt_pk_bf16_f32 v157, v157, v180
	ds_write_b16 v192, v156 offset:3808
	ds_write_b16_d16_hi v192, v156 offset:4080
	ds_write_b16 v192, v157 offset:21216
	ds_write_b16_d16_hi v192, v157 offset:21488
	v_cvt_pk_bf16_f32 v153, v153, v155
	v_mul_lo_u32 v154, v154, s60
	v_lshlrev_b32_e32 v155, 5, v0
	v_add3_u32 v154, s78, v154, v155
	ds_write_b128 v154, v[144:147] offset:34816
	ds_write_b128 v154, v[150:153] offset:34832
	s_and_saveexec_b64 s[0:1], vcc
	s_cbranch_execz .LBB0_426
	v_mul_f32_e32 v144, 0x3fb8aa3b, v149
	v_exp_f32_e32 v144, v144
	v_add_u32_e32 v145, s78, v148
	v_add_u32_e32 v145, 0x11800, v145
	ds_write_b32 v145, v144

.LBB0_435:
	s_setprio 2
	v_mov_b32_e32 v0, v214
	v_and_b32_e32 v164, 31, v0
	v_bfe_u32 v165, v0, 5, 1
	v_or_b32_e32 v0, s37, v164
	v_mov_b32_e32 v10, s76
	v_mad_u32_u24 v135, v0, s64, v10
	v_lshlrev_b32_e32 v133, 4, v165
	v_add_u32_e32 v10, v135, v133
	ds_read_b128 v[120:123], v10
	ds_read_b128 v[116:119], v10 offset:32
	ds_read_b128 v[112:115], v10 offset:64
	ds_read_b128 v[108:111], v10 offset:96
	ds_read_b128 v[104:107], v10 offset:128
	ds_read_b128 v[100:103], v10 offset:160
	ds_read_b128 v[96:99], v10 offset:192
	ds_read_b128 v[10:13], v10 offset:224
	v_or_b32_e32 v80, s8, v164
	v_mul_lo_u32 v80, v80, s60
	v_add_u32_e32 v134, s76, v80
	v_lshlrev_b32_e32 v166, 3, v165
	v_add_u32_e32 v132, s76, v133
	v_add_u32_e32 v124, v134, v166
	s_mov_b64 s[0:1], -1
	s_and_b64 vcc, exec, s[10:11]
	s_cbranch_vccz .LBB0_443
	v_mad_u32_u24 v84, v164, s64, v132
	ds_read_b128 v[80:83], v84 offset:17408
	ds_read_b128 v[126:129], v84 offset:17440
	ds_read_b128 v[136:139], v84 offset:17472
	ds_read_b128 v[140:143], v84 offset:17504
	ds_read_b128 v[144:147], v84 offset:17536
	ds_read_b128 v[148:151], v84 offset:17568
	ds_read_b128 v[152:155], v84 offset:17600
	ds_read_b128 v[156:159], v84 offset:17632
	v_add_u32_e32 v84, 0xd000, v124
	ds_read2_b64 v[160:163], v84 offset1:2
	ds_read2_b64 v[168:171], v84 offset0:4 offset1:6
	s_waitcnt lgkmcnt(0)
	s_waitcnt lgkmcnt(9)
	v_mfma_f32_32x32x16_bf16 v[80:95], v[80:83], v[120:123], 0
	s_waitcnt lgkmcnt(8)
	v_mfma_f32_32x32x16_bf16 v[80:95], v[126:129], v[116:119], v[80:95]
	s_waitcnt lgkmcnt(7)
	v_mfma_f32_32x32x16_bf16 v[80:95], v[136:139], v[112:115], v[80:95]
	s_waitcnt lgkmcnt(6)
	v_mfma_f32_32x32x16_bf16 v[80:95], v[140:143], v[108:111], v[80:95]
	s_waitcnt lgkmcnt(5)
	v_mfma_f32_32x32x16_bf16 v[80:95], v[144:147], v[104:107], v[80:95]
	s_waitcnt lgkmcnt(4)
	v_mfma_f32_32x32x16_bf16 v[80:95], v[148:151], v[100:103], v[80:95]
	s_waitcnt lgkmcnt(3)
	v_mfma_f32_32x32x16_bf16 v[80:95], v[152:155], v[96:99], v[80:95]
	s_waitcnt lgkmcnt(2)
	v_mfma_f32_32x32x16_bf16 v[80:95], v[156:159], v[10:13], v[80:95]
	s_nop 11
	v_cvt_pk_bf16_f32 v80, v80, v81
	v_cvt_pk_bf16_f32 v81, v82, v83
	v_cvt_pk_bf16_f32 v82, v84, v85
	v_cvt_pk_bf16_f32 v83, v86, v87
	s_waitcnt lgkmcnt(1)
	s_nop 0
	v_mfma_f32_32x32x16_bf16 v[144:159], v[160:163], v[80:83], 0
	v_cvt_pk_bf16_f32 v80, v88, v89
	v_cvt_pk_bf16_f32 v81, v90, v91
	v_cvt_pk_bf16_f32 v82, v92, v93
	v_cvt_pk_bf16_f32 v83, v94, v95
	s_waitcnt lgkmcnt(0)
	s_nop 0
	v_mfma_f32_32x32x16_bf16 v[144:159], v[168:171], v[80:83], v[144:159]
	s_mov_b32 s0, 1
	s_cbranch_execnz .LBB0_438
